# v16 plus packed LN sum chain and packed 1.0-adds in silu
# baseline (speedup 1.0000x reference)
.LBB1_6:
	s_waitcnt vmcnt(14)
	ds_write_b128 v119, v[38:41]
	s_waitcnt vmcnt(13)
	ds_write_b128 v119, v[42:45] offset:2304
	s_waitcnt vmcnt(12)
	ds_write_b128 v119, v[46:49] offset:4608
	s_waitcnt vmcnt(11)
	ds_write_b128 v119, v[50:53] offset:6912
	ds_bpermute_b32 v42, v107, v64
	ds_bpermute_b32 v43, v109, v64
	ds_bpermute_b32 v44, v110, v64
	v_add_u32_e32 v0, 0x1000, v62
	ds_bpermute_b32 v50, v111, v64
	v_min_i32_e32 v0, 0x927b, v0
	v_lshl_or_b32 v40, v0, 4, v106
	s_waitcnt lgkmcnt(3)
	v_lshlrev_b32_e32 v0, 7, v42
	v_ashrrev_i32_e32 v65, 31, v64
	v_lshl_add_u64 v[46:47], v[98:99], 0, v[0:1]
	s_waitcnt lgkmcnt(2)
	v_lshlrev_b32_e32 v0, 7, v43
	v_lshl_add_u64 v[38:39], v[64:65], 2, v[96:97]
	v_ashrrev_i32_e32 v41, 31, v40
	v_lshl_add_u64 v[48:49], v[98:99], 0, v[0:1]
	s_waitcnt lgkmcnt(1)
	v_lshlrev_b32_e32 v0, 7, v44
	s_waitcnt vmcnt(10)
	ds_bpermute_b32 v68, v114, v108
	ds_bpermute_b32 v66, v115, v108
	global_load_dword v108, v[38:39], off
	v_lshl_add_u64 v[38:39], v[40:41], 2, v[94:95]
	v_lshl_add_u64 v[64:65], v[100:101], 0, v[0:1]
	s_waitcnt lgkmcnt(2)
	v_lshlrev_b32_e32 v0, 7, v50
	global_load_dword v135, v[38:39], off
	s_nop 0
	global_load_dwordx4 v[38:41], v[46:47], off
	global_load_dwordx4 v[42:45], v[48:49], off
	v_lshl_add_u64 v[70:71], v[100:101], 0, v[0:1]
	global_load_dwordx4 v[46:49], v[64:65], off
	global_load_dwordx4 v[50:53], v[70:71], off
	ds_read_b128 v[70:73], v120
	ds_read_b128 v[74:77], v120 offset:64
	ds_read_b128 v[78:81], v120 offset:4608
	ds_read_b128 v[82:85], v120 offset:4672
	v_add_u32_e32 v0, 0x800, v62
	ds_write_b128 v121, v[2:5]
	ds_write_b128 v121, v[6:9] offset:1088
	ds_write_b128 v121, v[10:13] offset:2176
	ds_write_b128 v121, v[14:17] offset:3264
	ds_write_b128 v121, v[18:21] offset:4352
	ds_write_b128 v121, v[22:25] offset:5440
	s_waitcnt vmcnt(15)
	ds_write_b128 v121, v[26:29] offset:6528
	s_waitcnt vmcnt(14)
	ds_write_b128 v121, v[30:33] offset:7616
	ds_write_b128 v122, v[34:37] offset:8704
	v_min_i32_e32 v2, 0x927b, v0
	v_ashrrev_i32_e32 v3, 31, v2
	v_lshlrev_b64 v[4:5], 13, v[2:3]
	v_lshlrev_b64 v[2:3], 10, v[2:3]
	v_lshl_add_u64 v[18:19], v[102:103], 0, v[4:5]
	v_lshl_add_u64 v[62:63], v[104:105], 0, v[2:3]
	v_add_co_u32_e32 v64, vcc, s3, v18
	global_load_dwordx4 v[2:5], v[18:19], off nt
	global_load_dwordx4 v[6:9], v[18:19], off offset:1024 nt
	global_load_dwordx4 v[10:13], v[18:19], off offset:2048 nt
	global_load_dwordx4 v[14:17], v[18:19], off offset:3072 nt
	v_addc_co_u32_e32 v65, vcc, 0, v19, vcc
	global_load_dwordx4 v[34:37], v[62:63], off nt
	global_load_dwordx4 v[18:21], v[64:65], off nt
	global_load_dwordx4 v[22:25], v[64:65], off offset:1024 nt
	global_load_dwordx4 v[26:29], v[64:65], off offset:2048 nt
	global_load_dwordx4 v[30:33], v[64:65], off offset:3072 nt
	s_waitcnt lgkmcnt(13)
	v_add_f32_e32 v67, v68, v66
	v_mul_f32_e32 v184, 0xc3000000, v67
	s_waitcnt lgkmcnt(12)
	v_cvt_f32_ubyte3_e32 v169, v70
	v_cvt_f32_ubyte2_e32 v168, v70
	v_cvt_f32_ubyte1_e32 v171, v70
	v_cvt_f32_ubyte0_e32 v170, v70
	ds_read_b128 v[62:65], v123
	ds_read_b128 v[86:89], v123 offset:64
	ds_read_b128 v[90:93], v112
	ds_read_b128 v[136:139], v112 offset:4608
	ds_read_b128 v[140:143], v112 offset:9216
	ds_read_b128 v[144:147], v112 offset:13824
	ds_read_b128 v[148:151], v112 offset:18432
	ds_read_b128 v[152:155], v112 offset:23040
	ds_read_b128 v[156:159], v112 offset:27648
	ds_read_b128 v[160:163], v112 offset:32256
	s_waitcnt lgkmcnt(14)
	v_cvt_f32_ubyte1_e32 v165, v78
	v_cvt_f32_ubyte0_e32 v164, v78
	v_cvt_f32_ubyte3_e32 v167, v78
	v_cvt_f32_ubyte2_e32 v166, v78
	v_pk_fma_f32 v[170:171], v[170:171], v[68:69], v[184:185] op_sel_hi:[1,0,0]
	v_pk_fma_f32 v[168:169], v[168:169], v[68:69], v[184:185] op_sel_hi:[1,0,0]
	v_pk_fma_f32 v[164:165], v[164:165], v[66:67], v[170:171] op_sel_hi:[1,0,1]
	v_pk_fma_f32 v[166:167], v[166:167], v[66:67], v[168:169] op_sel_hi:[1,0,1]
	v_cvt_f32_ubyte1_e32 v169, v79
	v_cvt_f32_ubyte0_e32 v168, v79
	v_cvt_f32_ubyte3_e32 v171, v79
	v_cvt_f32_ubyte2_e32 v170, v79
	v_cvt_f32_ubyte3_e32 v79, v71
	v_cvt_f32_ubyte2_e32 v78, v71
	v_cvt_f32_ubyte1_e32 v173, v71
	v_cvt_f32_ubyte0_e32 v172, v71
	v_pk_fma_f32 v[70:71], v[172:173], v[68:69], v[184:185] op_sel_hi:[1,0,0]
	v_pk_fma_f32 v[78:79], v[78:79], v[68:69], v[184:185] op_sel_hi:[1,0,0]
	v_cvt_f32_ubyte3_e32 v173, v72
	v_cvt_f32_ubyte2_e32 v172, v72
	v_cvt_f32_ubyte1_e32 v175, v72
	v_cvt_f32_ubyte0_e32 v174, v72
	v_pk_fma_f32 v[170:171], v[170:171], v[66:67], v[78:79] op_sel_hi:[1,0,1]
	v_pk_fma_f32 v[168:169], v[168:169], v[66:67], v[70:71] op_sel_hi:[1,0,1]
	v_cvt_f32_ubyte1_e32 v71, v80
	v_cvt_f32_ubyte0_e32 v70, v80
	v_cvt_f32_ubyte3_e32 v79, v80
	v_cvt_f32_ubyte2_e32 v78, v80
	v_pk_fma_f32 v[176:177], v[174:175], v[68:69], v[184:185] op_sel_hi:[1,0,0]
	v_pk_fma_f32 v[172:173], v[172:173], v[68:69], v[184:185] op_sel_hi:[1,0,0]
	v_cvt_f32_ubyte2_e32 v80, v73
	v_pk_fma_f32 v[174:175], v[78:79], v[66:67], v[172:173] op_sel_hi:[1,0,1]
	v_pk_fma_f32 v[172:173], v[70:71], v[66:67], v[176:177] op_sel_hi:[1,0,1]
	v_cvt_f32_ubyte1_e32 v177, v73
	v_cvt_f32_ubyte0_e32 v176, v73
	v_cvt_f32_ubyte1_e32 v71, v81
	v_cvt_f32_ubyte0_e32 v70, v81
	v_cvt_f32_ubyte3_e32 v79, v81
	v_cvt_f32_ubyte2_e32 v78, v81
	v_cvt_f32_ubyte3_e32 v81, v73
	v_pk_fma_f32 v[176:177], v[176:177], v[68:69], v[184:185] op_sel_hi:[1,0,0]
	v_pk_fma_f32 v[72:73], v[80:81], v[68:69], v[184:185] op_sel_hi:[1,0,0]
	v_pk_fma_f32 v[70:71], v[70:71], v[66:67], v[176:177] op_sel_hi:[1,0,1]
	v_cvt_f32_ubyte3_e32 v177, v74
	v_cvt_f32_ubyte2_e32 v176, v74
	v_cvt_f32_ubyte1_e32 v179, v74
	v_cvt_f32_ubyte0_e32 v178, v74
	v_pk_fma_f32 v[72:73], v[78:79], v[66:67], v[72:73] op_sel_hi:[1,0,1]
	v_cvt_f32_ubyte1_e32 v79, v82
	v_cvt_f32_ubyte0_e32 v78, v82
	v_cvt_f32_ubyte3_e32 v81, v82
	v_cvt_f32_ubyte2_e32 v80, v82
	v_pk_fma_f32 v[178:179], v[178:179], v[68:69], v[184:185] op_sel_hi:[1,0,0]
	v_pk_fma_f32 v[176:177], v[176:177], v[68:69], v[184:185] op_sel_hi:[1,0,0]
	v_pk_fma_f32 v[78:79], v[78:79], v[66:67], v[178:179] op_sel_hi:[1,0,1]
	v_pk_fma_f32 v[80:81], v[80:81], v[66:67], v[176:177] op_sel_hi:[1,0,1]
	v_cvt_f32_ubyte1_e32 v177, v83
	v_cvt_f32_ubyte0_e32 v176, v83
	v_cvt_f32_ubyte3_e32 v179, v83
	v_cvt_f32_ubyte2_e32 v178, v83
	v_cvt_f32_ubyte3_e32 v83, v75
	v_cvt_f32_ubyte2_e32 v82, v75
	v_cvt_f32_ubyte1_e32 v181, v75
	v_cvt_f32_ubyte0_e32 v180, v75
	v_pk_fma_f32 v[74:75], v[180:181], v[68:69], v[184:185] op_sel_hi:[1,0,0]
	v_pk_fma_f32 v[82:83], v[82:83], v[68:69], v[184:185] op_sel_hi:[1,0,0]
	v_cvt_f32_ubyte3_e32 v181, v76
	v_cvt_f32_ubyte2_e32 v180, v76
	v_cvt_f32_ubyte1_e32 v183, v76
	v_cvt_f32_ubyte0_e32 v182, v76
	v_pk_fma_f32 v[178:179], v[178:179], v[66:67], v[82:83] op_sel_hi:[1,0,1]
	v_pk_fma_f32 v[176:177], v[176:177], v[66:67], v[74:75] op_sel_hi:[1,0,1]
	v_cvt_f32_ubyte1_e32 v75, v84
	v_cvt_f32_ubyte0_e32 v74, v84
	v_cvt_f32_ubyte3_e32 v83, v84
	v_cvt_f32_ubyte2_e32 v82, v84
	v_pk_fma_f32 v[186:187], v[182:183], v[68:69], v[184:185] op_sel_hi:[1,0,0]
	v_pk_fma_f32 v[180:181], v[180:181], v[68:69], v[184:185] op_sel_hi:[1,0,0]
	v_cvt_f32_ubyte2_e32 v84, v77
	v_pk_fma_f32 v[182:183], v[82:83], v[66:67], v[180:181] op_sel_hi:[1,0,1]
	v_pk_fma_f32 v[180:181], v[74:75], v[66:67], v[186:187] op_sel_hi:[1,0,1]
	v_cvt_f32_ubyte1_e32 v75, v85
	v_cvt_f32_ubyte0_e32 v74, v85
	v_cvt_f32_ubyte3_e32 v83, v85
	v_cvt_f32_ubyte2_e32 v82, v85
	v_cvt_f32_ubyte3_e32 v85, v77
	v_cvt_f32_ubyte1_e32 v187, v77
	v_cvt_f32_ubyte0_e32 v186, v77
	v_pk_fma_f32 v[76:77], v[186:187], v[68:69], v[184:185] op_sel_hi:[1,0,0]
	v_pk_fma_f32 v[68:69], v[84:85], v[68:69], v[184:185] op_sel_hi:[1,0,0]
	s_nop 0
	v_pk_fma_f32 v[68:69], v[82:83], v[66:67], v[68:69] op_sel_hi:[1,0,1]
	v_pk_fma_f32 v[66:67], v[74:75], v[66:67], v[76:77] op_sel_hi:[1,0,1]
	ds_read_b128 v[74:77], v123 offset:128
	ds_read_b128 v[82:85], v123 offset:192
	ds_read_b128 v[184:187], v112 offset:64
	ds_read_b128 v[188:191], v112 offset:4672
	ds_read_b128 v[192:195], v112 offset:9280
	ds_read_b128 v[196:199], v112 offset:13888
	ds_read_b128 v[200:203], v112 offset:18496
	ds_read_b128 v[204:207], v112 offset:23104
	ds_read_b128 v[208:211], v112 offset:27712
	ds_read_b128 v[212:215], v112 offset:32320
	s_waitcnt lgkmcnt(14)
	v_cvt_pk_bf16_f32 v62, v62, v63
	v_cvt_pk_bf16_f32 v63, v64, v65
	v_cvt_pk_bf16_f32 v64, v86, v87
	v_cvt_pk_bf16_f32 v65, v88, v89
	s_nop 1
	v_mfma_f32_16x16x32_bf16 v[86:89], v[90:93], v[62:65], v[164:167]
	v_mfma_f32_16x16x32_bf16 v[90:93], v[136:139], v[62:65], v[168:171]
	v_mfma_f32_16x16x32_bf16 v[136:139], v[140:143], v[62:65], v[172:175]
	v_mfma_f32_16x16x32_bf16 v[70:73], v[144:147], v[62:65], v[70:73]
	s_waitcnt lgkmcnt(13)
	v_mfma_f32_16x16x32_bf16 v[78:81], v[148:151], v[62:65], v[78:81]
	s_waitcnt lgkmcnt(12)
	v_mfma_f32_16x16x32_bf16 v[140:143], v[152:155], v[62:65], v[176:179]
	s_waitcnt lgkmcnt(11)
	v_mfma_f32_16x16x32_bf16 v[144:147], v[156:159], v[62:65], v[180:183]
	s_waitcnt lgkmcnt(10)
	v_mfma_f32_16x16x32_bf16 v[62:65], v[160:163], v[62:65], v[66:69]
	s_nop 2
	ds_read_b128 v[66:69], v123 offset:256
	ds_read_b128 v[148:151], v123 offset:320
	ds_read_b128 v[152:155], v112 offset:128
	ds_read_b128 v[156:159], v112 offset:4736
	ds_read_b128 v[160:163], v112 offset:9344
	ds_read_b128 v[164:167], v112 offset:13952
	ds_read_b128 v[168:171], v112 offset:18560
	ds_read_b128 v[172:175], v112 offset:23168
	ds_read_b128 v[176:179], v112 offset:27776
	ds_read_b128 v[180:183], v112 offset:32384
	s_waitcnt lgkmcnt(14)
	v_cvt_pk_bf16_f32 v74, v74, v75
	v_cvt_pk_bf16_f32 v75, v76, v77
	v_cvt_pk_bf16_f32 v76, v82, v83
	v_cvt_pk_bf16_f32 v77, v84, v85
	s_waitcnt lgkmcnt(10)
	s_nop 0
	v_mfma_f32_16x16x32_bf16 v[62:65], v[212:215], v[74:77], v[62:65]
	v_mfma_f32_16x16x32_bf16 v[82:85], v[184:187], v[74:77], v[86:89]
	v_mfma_f32_16x16x32_bf16 v[86:89], v[188:191], v[74:77], v[90:93]
	v_mfma_f32_16x16x32_bf16 v[90:93], v[192:195], v[74:77], v[136:139]
	v_mfma_f32_16x16x32_bf16 v[70:73], v[196:199], v[74:77], v[70:73]
	v_mfma_f32_16x16x32_bf16 v[78:81], v[200:203], v[74:77], v[78:81]
	v_mfma_f32_16x16x32_bf16 v[136:139], v[204:207], v[74:77], v[140:143]
	v_mfma_f32_16x16x32_bf16 v[140:143], v[208:211], v[74:77], v[144:147]
	ds_read_b128 v[74:77], v123 offset:384
	s_nop 1
	ds_read_b128 v[144:147], v123 offset:448
	ds_read_b128 v[184:187], v112 offset:192
	ds_read_b128 v[188:191], v112 offset:4800
	ds_read_b128 v[192:195], v112 offset:9408
	ds_read_b128 v[196:199], v112 offset:14016
	ds_read_b128 v[200:203], v112 offset:18624
	ds_read_b128 v[204:207], v112 offset:23232
	ds_read_b128 v[208:211], v112 offset:27840
	ds_read_b128 v[212:215], v112 offset:32448
	s_waitcnt lgkmcnt(14)
	v_cvt_pk_bf16_f32 v66, v66, v67
	v_cvt_pk_bf16_f32 v67, v68, v69
	v_cvt_pk_bf16_f32 v68, v148, v149
	v_cvt_pk_bf16_f32 v69, v150, v151
	s_waitcnt lgkmcnt(10)
	s_nop 0
	v_mfma_f32_16x16x32_bf16 v[62:65], v[180:183], v[66:69], v[62:65]
	v_mfma_f32_16x16x32_bf16 v[82:85], v[152:155], v[66:69], v[82:85]
	v_mfma_f32_16x16x32_bf16 v[86:89], v[156:159], v[66:69], v[86:89]
	v_mfma_f32_16x16x32_bf16 v[90:93], v[160:163], v[66:69], v[90:93]
	v_mfma_f32_16x16x32_bf16 v[70:73], v[164:167], v[66:69], v[70:73]
	v_mfma_f32_16x16x32_bf16 v[78:81], v[168:171], v[66:69], v[78:81]
	v_mfma_f32_16x16x32_bf16 v[136:139], v[172:175], v[66:69], v[136:139]
	v_mfma_f32_16x16x32_bf16 v[140:143], v[176:179], v[66:69], v[140:143]
	ds_read2st64_b64 v[66:69], v134 offset0:54 offset1:63
	ds_read2st64_b64 v[148:151], v134 offset0:36 offset1:45
	ds_read2st64_b64 v[152:155], v134 offset0:18 offset1:27
	ds_read2st64_b64 v[156:159], v134 offset1:9
	ds_read_b128 v[160:163], v124 offset:8704
	s_waitcnt lgkmcnt(14)
	v_cvt_pk_bf16_f32 v74, v74, v75
	v_cvt_pk_bf16_f32 v75, v76, v77
	s_waitcnt lgkmcnt(13)
	v_cvt_pk_bf16_f32 v76, v144, v145
	v_cvt_pk_bf16_f32 v77, v146, v147
	s_waitcnt lgkmcnt(5)
	s_nop 0
	v_mfma_f32_16x16x32_bf16 v[62:65], v[212:215], v[74:77], v[62:65]
	v_mfma_f32_16x16x32_bf16 v[82:85], v[184:187], v[74:77], v[82:85]
	v_mfma_f32_16x16x32_bf16 v[86:89], v[188:191], v[74:77], v[86:89]
	v_mfma_f32_16x16x32_bf16 v[90:93], v[192:195], v[74:77], v[90:93]
	v_mfma_f32_16x16x32_bf16 v[70:73], v[196:199], v[74:77], v[70:73]
	v_mfma_f32_16x16x32_bf16 v[78:81], v[200:203], v[74:77], v[78:81]
	v_mfma_f32_16x16x32_bf16 v[136:139], v[204:207], v[74:77], v[136:139]
	v_mfma_f32_16x16x32_bf16 v[140:143], v[208:211], v[74:77], v[140:143]
	ds_read_b128 v[144:147], v125
	ds_read_b128 v[164:167], v126
	ds_read_b128 v[168:171], v127
	ds_read_b128 v[172:175], v128
	ds_read_b128 v[176:179], v129
	ds_read_b128 v[180:183], v130
	ds_read_b128 v[184:187], v131
	ds_read_b128 v[188:191], v132
	ds_read_b128 v[192:195], v112 offset:36864
	ds_read_b128 v[196:199], v112 offset:41472
	ds_read_b128 v[200:203], v112 offset:46080
	ds_read_b128 v[204:207], v112 offset:50688
	ds_read_b128 v[208:211], v112 offset:55296
	ds_read_b128 v[212:215], v112 offset:59904
	ds_read_b128 v[216:219], v112 offset:64512
	ds_read_b128 v[220:223], v113 offset:32256
	s_waitcnt lgkmcnt(14)
	v_cvt_pk_bf16_f32 v74, v160, v161
	v_cvt_pk_bf16_f32 v75, v162, v163
	s_nop 1
	v_mfma_f32_16x16x16_bf16 v[160:163], v[156:157], v[74:75], v[82:85]
	v_mfma_f32_16x16x16_bf16 v[86:89], v[158:159], v[74:75], v[86:89]
	v_mfma_f32_16x16x16_bf16 v[90:93], v[152:153], v[74:75], v[90:93]
	v_mfma_f32_16x16x16_bf16 v[70:73], v[154:155], v[74:75], v[70:73]
	v_mfma_f32_16x16x16_bf16 v[78:81], v[148:149], v[74:75], v[78:81]
	v_mfma_f32_16x16x16_bf16 v[136:139], v[150:151], v[74:75], v[136:139]
	v_mfma_f32_16x16x16_bf16 v[82:85], v[66:67], v[74:75], v[140:143]
	v_mfma_f32_16x16x16_bf16 v[74:77], v[68:69], v[74:75], v[62:65]
	s_nop 2
	v_exp_f32_e32 v62, v160
	v_exp_f32_e32 v63, v161
	v_exp_f32_e32 v64, v162
	v_exp_f32_e32 v65, v163
	v_add_f32_e32 v62, 1.0, v62
	v_add_f32_e32 v63, 1.0, v63
	v_rcp_f32_e32 v62, v62
	v_rcp_f32_e32 v63, v63
	v_add_f32_e32 v64, 1.0, v64
	v_add_f32_e32 v65, 1.0, v65
	v_rcp_f32_e32 v64, v64
	v_rcp_f32_e32 v65, v65
	v_pk_mul_f32 v[62:63], v[160:161], v[62:63]
	v_exp_f32_e32 v66, v86
	v_cvt_pk_bf16_f32 v140, v62, v63
	v_pk_mul_f32 v[62:63], v[162:163], v[64:65]
	v_exp_f32_e32 v64, v88
	v_cvt_pk_bf16_f32 v141, v62, v63
	v_exp_f32_e32 v63, v87
	v_exp_f32_e32 v65, v89
	v_add_f32_e32 v62, 1.0, v66
	v_rcp_f32_e32 v62, v62
	v_add_f32_e32 v63, 1.0, v63
	v_rcp_f32_e32 v63, v63
	v_add_f32_e32 v64, 1.0, v64
	v_add_f32_e32 v65, 1.0, v65
	v_rcp_f32_e32 v64, v64
	v_rcp_f32_e32 v65, v65
	v_pk_mul_f32 v[62:63], v[86:87], v[62:63]
	v_exp_f32_e32 v66, v90
	v_cvt_pk_bf16_f32 v142, v62, v63
	v_pk_mul_f32 v[62:63], v[88:89], v[64:65]
	v_exp_f32_e32 v64, v92
	v_cvt_pk_bf16_f32 v143, v62, v63
	v_exp_f32_e32 v63, v91
	v_exp_f32_e32 v65, v93
	v_add_f32_e32 v62, 1.0, v66
	v_rcp_f32_e32 v62, v62
	v_add_f32_e32 v63, 1.0, v63
	v_rcp_f32_e32 v63, v63
	v_add_f32_e32 v64, 1.0, v64
	v_add_f32_e32 v65, 1.0, v65
	v_rcp_f32_e32 v64, v64
	v_rcp_f32_e32 v65, v65
	v_pk_mul_f32 v[62:63], v[90:91], v[62:63]
	v_exp_f32_e32 v66, v70
	v_cvt_pk_bf16_f32 v86, v62, v63
	v_pk_mul_f32 v[62:63], v[92:93], v[64:65]
	v_exp_f32_e32 v64, v72
	v_cvt_pk_bf16_f32 v87, v62, v63
	v_exp_f32_e32 v63, v71
	v_exp_f32_e32 v65, v73
	v_add_f32_e32 v62, 1.0, v66
	v_rcp_f32_e32 v62, v62
	v_add_f32_e32 v63, 1.0, v63
	v_rcp_f32_e32 v63, v63
	v_add_f32_e32 v64, 1.0, v64
	v_add_f32_e32 v65, 1.0, v65
	v_rcp_f32_e32 v64, v64
	v_rcp_f32_e32 v65, v65
	v_pk_mul_f32 v[62:63], v[70:71], v[62:63]
	v_exp_f32_e32 v66, v78
	v_cvt_pk_bf16_f32 v88, v62, v63
	v_pk_mul_f32 v[62:63], v[72:73], v[64:65]
	v_exp_f32_e32 v64, v80
	v_cvt_pk_bf16_f32 v89, v62, v63
	v_exp_f32_e32 v63, v79
	v_exp_f32_e32 v65, v81
	v_add_f32_e32 v62, 1.0, v66
	v_rcp_f32_e32 v62, v62
	v_add_f32_e32 v63, 1.0, v63
	v_rcp_f32_e32 v63, v63
	v_add_f32_e32 v64, 1.0, v64
	v_add_f32_e32 v65, 1.0, v65
	v_rcp_f32_e32 v64, v64
	v_rcp_f32_e32 v65, v65
	v_exp_f32_e32 v66, v136
	v_pk_mul_f32 v[62:63], v[78:79], v[62:63]
	v_exp_f32_e32 v67, v139
	v_cvt_pk_bf16_f32 v148, v62, v63
	v_pk_mul_f32 v[62:63], v[80:81], v[64:65]
	v_exp_f32_e32 v65, v137
	v_add_f32_e32 v64, 1.0, v66
	v_exp_f32_e32 v66, v138
	v_rcp_f32_e32 v64, v64
	v_add_f32_e32 v65, 1.0, v65
	v_rcp_f32_e32 v65, v65
	v_add_f32_e32 v66, 1.0, v66
	v_add_f32_e32 v67, 1.0, v67
	v_rcp_f32_e32 v66, v66
	v_rcp_f32_e32 v67, v67
	v_cvt_pk_bf16_f32 v149, v62, v63
	v_pk_mul_f32 v[62:63], v[136:137], v[64:65]
	s_nop 0
	v_cvt_pk_bf16_f32 v150, v62, v63
	v_pk_mul_f32 v[62:63], v[138:139], v[66:67]
	s_nop 0
	v_cvt_pk_bf16_f32 v151, v62, v63
	ds_read_b128 v[90:93], v112 offset:36928
	ds_read_b128 v[136:139], v112 offset:41536
	ds_read_b128 v[152:155], v112 offset:46144
	ds_read_b128 v[156:159], v112 offset:50752
	ds_read_b128 v[160:163], v112 offset:55360
	ds_read_b128 v[224:227], v112 offset:59968
	ds_read_b128 v[228:231], v112 offset:64576
	ds_read_b128 v[232:235], v113 offset:32320
	ds_read_b128 v[62:65], v123
	ds_read_b128 v[66:69], v123 offset:64
	s_waitcnt lgkmcnt(14)
	v_mfma_f32_16x16x32_bf16 v[144:147], v[192:195], v[140:143], v[144:147]
	v_mfma_f32_16x16x32_bf16 v[164:167], v[196:199], v[140:143], v[164:167]
	v_mfma_f32_16x16x32_bf16 v[168:171], v[200:203], v[140:143], v[168:171]
	v_mfma_f32_16x16x32_bf16 v[172:175], v[204:207], v[140:143], v[172:175]
	s_waitcnt lgkmcnt(13)
	v_mfma_f32_16x16x32_bf16 v[176:179], v[208:211], v[140:143], v[176:179]
	s_waitcnt lgkmcnt(12)
	v_mfma_f32_16x16x32_bf16 v[180:183], v[212:215], v[140:143], v[180:183]
	s_waitcnt lgkmcnt(11)
	v_mfma_f32_16x16x32_bf16 v[184:187], v[216:219], v[140:143], v[184:187]
	s_waitcnt lgkmcnt(10)
	v_mfma_f32_16x16x32_bf16 v[140:143], v[220:223], v[140:143], v[188:191]
	s_nop 2
	ds_read_b128 v[188:191], v112 offset:36992
	ds_read_b128 v[192:195], v112 offset:41600
	ds_read_b128 v[196:199], v112 offset:46208
	ds_read_b128 v[200:203], v112 offset:50816
	ds_read_b128 v[204:207], v112 offset:55424
	ds_read_b128 v[208:211], v112 offset:60032
	ds_read_b128 v[212:215], v112 offset:64640
	ds_read_b128 v[216:219], v113 offset:32384
	ds_read_b128 v[70:73], v123 offset:128
	ds_read_b128 v[78:81], v123 offset:192
	s_waitcnt lgkmcnt(14)
	v_mfma_f32_16x16x32_bf16 v[144:147], v[90:93], v[86:89], v[144:147]
	v_mfma_f32_16x16x32_bf16 v[136:139], v[136:139], v[86:89], v[164:167]
	v_mfma_f32_16x16x32_bf16 v[152:155], v[152:155], v[86:89], v[168:171]
	v_mfma_f32_16x16x32_bf16 v[156:159], v[156:159], v[86:89], v[172:175]
	v_mfma_f32_16x16x32_bf16 v[160:163], v[160:163], v[86:89], v[176:179]
	v_mfma_f32_16x16x32_bf16 v[164:167], v[224:227], v[86:89], v[180:183]
	s_waitcnt lgkmcnt(13)
	v_mfma_f32_16x16x32_bf16 v[168:171], v[228:231], v[86:89], v[184:187]
	s_waitcnt lgkmcnt(12)
	v_mfma_f32_16x16x32_bf16 v[140:143], v[232:235], v[86:89], v[140:143]
	ds_read_b128 v[172:175], v112 offset:37056
	ds_read_b128 v[176:179], v112 offset:41664
	ds_read_b128 v[180:183], v112 offset:46272
	ds_read_b128 v[184:187], v112 offset:50880
	ds_read_b128 v[220:223], v112 offset:55488
	ds_read_b128 v[224:227], v112 offset:60096
	ds_read_b128 v[228:231], v112 offset:64704
	ds_read_b128 v[232:235], v113 offset:32448
	ds_read_b128 v[86:89], v123 offset:256
	ds_read_b128 v[90:93], v123 offset:320
	s_waitcnt lgkmcnt(14)
	v_mfma_f32_16x16x32_bf16 v[144:147], v[188:191], v[148:151], v[144:147]
	v_mfma_f32_16x16x32_bf16 v[136:139], v[192:195], v[148:151], v[136:139]
	v_mfma_f32_16x16x32_bf16 v[152:155], v[196:199], v[148:151], v[152:155]
	v_mfma_f32_16x16x32_bf16 v[156:159], v[200:203], v[148:151], v[156:159]
	v_mfma_f32_16x16x32_bf16 v[160:163], v[204:207], v[148:151], v[160:163]
	v_mfma_f32_16x16x32_bf16 v[164:167], v[208:211], v[148:151], v[164:167]
	s_waitcnt lgkmcnt(13)
	v_mfma_f32_16x16x32_bf16 v[168:171], v[212:215], v[148:151], v[168:171]
	s_waitcnt lgkmcnt(12)
	v_mfma_f32_16x16x32_bf16 v[140:143], v[216:219], v[148:151], v[140:143]
	v_exp_f32_e32 v148, v82
	v_exp_f32_e32 v149, v83
	v_exp_f32_e32 v150, v84
	v_exp_f32_e32 v151, v85
	v_add_f32_e32 v148, 1.0, v148
	v_add_f32_e32 v149, 1.0, v149
	v_rcp_f32_e32 v148, v148
	v_rcp_f32_e32 v149, v149
	v_add_f32_e32 v150, 1.0, v150
	v_add_f32_e32 v151, 1.0, v151
	v_rcp_f32_e32 v150, v150
	v_rcp_f32_e32 v151, v151
	v_pk_mul_f32 v[82:83], v[82:83], v[148:149]
	v_exp_f32_e32 v148, v74
	v_cvt_pk_bf16_f32 v82, v82, v83
	v_pk_mul_f32 v[84:85], v[84:85], v[150:151]
	v_exp_f32_e32 v149, v77
	v_cvt_pk_bf16_f32 v83, v84, v85
	v_exp_f32_e32 v85, v75
	v_add_f32_e32 v84, 1.0, v148
	v_exp_f32_e32 v148, v76
	v_rcp_f32_e32 v84, v84
	v_add_f32_e32 v85, 1.0, v85
	v_rcp_f32_e32 v85, v85
	v_add_f32_e32 v148, 1.0, v148
	v_rcp_f32_e32 v192, v148
	v_add_f32_e32 v148, 1.0, v149
	v_rcp_f32_e32 v193, v148
	ds_read_b128 v[148:151], v123 offset:384
	ds_read_b128 v[188:191], v123 offset:448
	v_pk_mul_f32 v[74:75], v[74:75], v[84:85]
	s_nop 0
	v_cvt_pk_bf16_f32 v84, v74, v75
	v_pk_mul_f32 v[74:75], v[76:77], v[192:193]
	s_nop 0
	v_cvt_pk_bf16_f32 v85, v74, v75
	s_waitcnt lgkmcnt(11)
	s_nop 0
	v_mfma_f32_16x16x32_bf16 v[74:77], v[172:175], v[82:85], v[144:147]
	s_waitcnt lgkmcnt(10)
	v_mfma_f32_16x16x32_bf16 v[136:139], v[176:179], v[82:85], v[136:139]
	s_waitcnt lgkmcnt(9)
	v_mfma_f32_16x16x32_bf16 v[144:147], v[180:183], v[82:85], v[152:155]
	s_waitcnt lgkmcnt(8)
	v_mfma_f32_16x16x32_bf16 v[152:155], v[184:187], v[82:85], v[156:159]
	s_waitcnt lgkmcnt(7)
	v_mfma_f32_16x16x32_bf16 v[156:159], v[220:223], v[82:85], v[160:163]
	s_waitcnt lgkmcnt(6)
	v_mfma_f32_16x16x32_bf16 v[160:163], v[224:227], v[82:85], v[164:167]
	s_waitcnt lgkmcnt(5)
	v_mfma_f32_16x16x32_bf16 v[164:167], v[228:231], v[82:85], v[168:171]
	s_waitcnt lgkmcnt(4)
	v_mfma_f32_16x16x32_bf16 v[82:85], v[232:235], v[82:85], v[140:143]
	s_nop 2
	v_exp_f32_e32 v140, v74
	v_exp_f32_e32 v141, v75
	v_exp_f32_e32 v168, v136
	v_exp_f32_e32 v169, v137
	v_exp_f32_e32 v170, v138
	v_exp_f32_e32 v171, v139
	v_exp_f32_e32 v142, v76
	v_exp_f32_e32 v143, v77
	v_add_f32_e32 v140, 1.0, v140
	v_add_f32_e32 v141, 1.0, v141
	v_rcp_f32_e32 v140, v140
	v_rcp_f32_e32 v141, v141
	v_add_f32_e32 v168, 1.0, v168
	v_add_f32_e32 v169, 1.0, v169
	v_rcp_f32_e32 v168, v168
	v_rcp_f32_e32 v169, v169
	v_pk_add_f32 v[170:171], v[170:171], 1.0 op_sel_hi:[1,0]
	v_pk_add_f32 v[142:143], v[142:143], 1.0 op_sel_hi:[1,0]
	v_rcp_f32_e32 v170, v170
	v_rcp_f32_e32 v171, v171
	v_rcp_f32_e32 v142, v142
	v_rcp_f32_e32 v143, v143
	v_exp_f32_e32 v172, v144
	v_exp_f32_e32 v173, v145
	v_pk_mul_f32 v[74:75], v[74:75], v[140:141]
	v_pk_mul_f32 v[136:137], v[136:137], v[168:169]
	v_pk_fma_f32 v[62:63], v[74:75], s[2:3], v[62:63] op_sel_hi:[1,0,1]
	v_exp_f32_e32 v174, v146
	v_pk_mul_f32 v[236:237], v[62:63], v[62:63]
	v_pk_add_f32 v[238:239], v[62:63], 0 op_sel_hi:[1,0]
	v_exp_f32_e32 v175, v147
	v_pk_fma_f32 v[66:67], v[136:137], s[2:3], v[66:67] op_sel_hi:[1,0,1]
	v_pk_mul_f32 v[136:137], v[138:139], v[170:171]
	v_pk_fma_f32 v[236:237], v[66:67], v[66:67], v[236:237]
	v_pk_add_f32 v[238:239], v[66:67], v[238:239]
	v_pk_fma_f32 v[68:69], v[136:137], s[2:3], v[68:69] op_sel_hi:[1,0,1]
	v_pk_mul_f32 v[74:75], v[76:77], v[142:143]
	v_pk_fma_f32 v[236:237], v[68:69], v[68:69], v[236:237]
	v_pk_add_f32 v[238:239], v[68:69], v[238:239]
	v_pk_add_f32 v[172:173], v[172:173], 1.0 op_sel_hi:[1,0]
	v_exp_f32_e32 v176, v152
	v_exp_f32_e32 v177, v153
	v_pk_fma_f32 v[64:65], v[74:75], s[2:3], v[64:65] op_sel_hi:[1,0,1]
	v_rcp_f32_e32 v172, v172
	v_pk_fma_f32 v[236:237], v[64:65], v[64:65], v[236:237]
	v_pk_add_f32 v[238:239], v[64:65], v[238:239]
	v_rcp_f32_e32 v173, v173
	v_pk_add_f32 v[174:175], v[174:175], 1.0 op_sel_hi:[1,0]
	v_exp_f32_e32 v178, v154
	v_exp_f32_e32 v179, v155
	v_rcp_f32_e32 v174, v174
	v_rcp_f32_e32 v175, v175
	v_pk_add_f32 v[176:177], v[176:177], 1.0 op_sel_hi:[1,0]
	v_exp_f32_e32 v180, v156
	v_exp_f32_e32 v181, v157
	v_rcp_f32_e32 v176, v176
	v_rcp_f32_e32 v177, v177
	v_pk_mul_f32 v[144:145], v[144:145], v[172:173]
	v_pk_add_f32 v[178:179], v[178:179], 1.0 op_sel_hi:[1,0]
	v_exp_f32_e32 v182, v158
	v_exp_f32_e32 v183, v159
	v_pk_fma_f32 v[70:71], v[144:145], s[2:3], v[70:71] op_sel_hi:[1,0,1]
	v_rcp_f32_e32 v178, v178
	v_pk_fma_f32 v[236:237], v[70:71], v[70:71], v[236:237]
	v_pk_add_f32 v[238:239], v[70:71], v[238:239]
	v_rcp_f32_e32 v179, v179
	v_pk_mul_f32 v[144:145], v[146:147], v[174:175]
	v_pk_add_f32 v[180:181], v[180:181], 1.0 op_sel_hi:[1,0]
	v_exp_f32_e32 v184, v160
	v_exp_f32_e32 v185, v161
	v_pk_fma_f32 v[72:73], v[144:145], s[2:3], v[72:73] op_sel_hi:[1,0,1]
	v_rcp_f32_e32 v180, v180
	v_pk_fma_f32 v[236:237], v[72:73], v[72:73], v[236:237]
	v_pk_add_f32 v[238:239], v[72:73], v[238:239]
	v_rcp_f32_e32 v181, v181
	v_pk_mul_f32 v[152:153], v[152:153], v[176:177]
	v_pk_add_f32 v[182:183], v[182:183], 1.0 op_sel_hi:[1,0]
	v_exp_f32_e32 v186, v162
	v_exp_f32_e32 v187, v163
	v_pk_fma_f32 v[78:79], v[152:153], s[2:3], v[78:79] op_sel_hi:[1,0,1]
	v_rcp_f32_e32 v182, v182
	v_pk_fma_f32 v[236:237], v[78:79], v[78:79], v[236:237]
	v_pk_add_f32 v[238:239], v[78:79], v[238:239]
	v_rcp_f32_e32 v183, v183
	v_pk_mul_f32 v[152:153], v[154:155], v[178:179]
	v_pk_add_f32 v[184:185], v[184:185], 1.0 op_sel_hi:[1,0]
	v_exp_f32_e32 v192, v164
	v_exp_f32_e32 v193, v165
	v_pk_fma_f32 v[80:81], v[152:153], s[2:3], v[80:81] op_sel_hi:[1,0,1]
	v_rcp_f32_e32 v184, v184
	v_pk_fma_f32 v[236:237], v[80:81], v[80:81], v[236:237]
	v_pk_add_f32 v[238:239], v[80:81], v[238:239]
	v_rcp_f32_e32 v185, v185
	v_pk_mul_f32 v[156:157], v[156:157], v[180:181]
	v_pk_add_f32 v[186:187], v[186:187], 1.0 op_sel_hi:[1,0]
	v_exp_f32_e32 v194, v166
	v_exp_f32_e32 v195, v167
	s_waitcnt lgkmcnt(3)
	v_pk_fma_f32 v[86:87], v[156:157], s[2:3], v[86:87] op_sel_hi:[1,0,1]
	v_rcp_f32_e32 v186, v186
	v_pk_fma_f32 v[236:237], v[86:87], v[86:87], v[236:237]
	v_pk_add_f32 v[238:239], v[86:87], v[238:239]
	v_rcp_f32_e32 v187, v187
	v_pk_mul_f32 v[156:157], v[158:159], v[182:183]
	v_pk_add_f32 v[192:193], v[192:193], 1.0 op_sel_hi:[1,0]
	v_exp_f32_e32 v196, v82
	v_exp_f32_e32 v197, v83
	v_pk_fma_f32 v[88:89], v[156:157], s[2:3], v[88:89] op_sel_hi:[1,0,1]
	v_rcp_f32_e32 v192, v192
	v_pk_fma_f32 v[236:237], v[88:89], v[88:89], v[236:237]
	v_pk_add_f32 v[238:239], v[88:89], v[238:239]
	v_rcp_f32_e32 v193, v193
	v_pk_mul_f32 v[160:161], v[160:161], v[184:185]
	v_pk_add_f32 v[194:195], v[194:195], 1.0 op_sel_hi:[1,0]
	v_exp_f32_e32 v198, v84
	v_exp_f32_e32 v199, v85
	s_waitcnt lgkmcnt(2)
	v_pk_fma_f32 v[90:91], v[160:161], s[2:3], v[90:91] op_sel_hi:[1,0,1]
	v_rcp_f32_e32 v194, v194
	v_pk_fma_f32 v[236:237], v[90:91], v[90:91], v[236:237]
	v_pk_add_f32 v[238:239], v[90:91], v[238:239]
	v_rcp_f32_e32 v195, v195
	v_pk_mul_f32 v[160:161], v[162:163], v[186:187]
	v_pk_add_f32 v[196:197], v[196:197], 1.0 op_sel_hi:[1,0]
	v_pk_fma_f32 v[92:93], v[160:161], s[2:3], v[92:93] op_sel_hi:[1,0,1]
	v_rcp_f32_e32 v196, v196
	v_pk_fma_f32 v[236:237], v[92:93], v[92:93], v[236:237]
	v_pk_add_f32 v[238:239], v[92:93], v[238:239]
	v_rcp_f32_e32 v197, v197
	v_pk_mul_f32 v[164:165], v[164:165], v[192:193]
	v_pk_add_f32 v[198:199], v[198:199], 1.0 op_sel_hi:[1,0]
	s_waitcnt lgkmcnt(1)
	v_pk_fma_f32 v[148:149], v[164:165], s[2:3], v[148:149] op_sel_hi:[1,0,1]
	v_rcp_f32_e32 v198, v198
	v_pk_fma_f32 v[236:237], v[148:149], v[148:149], v[236:237]
	v_pk_add_f32 v[238:239], v[148:149], v[238:239]
	v_rcp_f32_e32 v199, v199
	v_pk_mul_f32 v[164:165], v[166:167], v[194:195]
	s_nop 0
	v_pk_fma_f32 v[150:151], v[164:165], s[2:3], v[150:151] op_sel_hi:[1,0,1]
	v_pk_mul_f32 v[82:83], v[82:83], v[196:197]
	v_pk_fma_f32 v[236:237], v[150:151], v[150:151], v[236:237]
	v_pk_add_f32 v[238:239], v[150:151], v[238:239]
	s_waitcnt lgkmcnt(0)
	v_pk_fma_f32 v[82:83], v[82:83], s[2:3], v[188:189] op_sel_hi:[1,0,1]
	v_pk_mul_f32 v[84:85], v[84:85], v[198:199]
	v_pk_fma_f32 v[236:237], v[82:83], v[82:83], v[236:237]
	v_pk_fma_f32 v[84:85], v[84:85], s[2:3], v[190:191] op_sel_hi:[1,0,1]
	v_pk_add_f32 v[238:239], v[82:83], v[238:239]
	v_pk_fma_f32 v[236:237], v[84:85], v[84:85], v[236:237]
	v_pk_add_f32 v[238:239], v[84:85], v[238:239]
	v_add_f32_e32 v75, v236, v237
	v_add_f32_e32 v74, v238, v239
	s_nop 1
	v_permlane16_swap_b32_e32 v74, v75
	s_nop 0
	v_add_f32_e32 v74, v74, v75
	v_mov_b32_e32 v75, v74
	s_nop 1
	v_permlane32_swap_b32_e32 v74, v75
	s_nop 0
	v_add_f32_e32 v74, v74, v75
	v_mov_b32_e32 v75, v74
	s_nop 1
	v_permlane16_swap_b32_e32 v74, v75
	s_nop 0
	v_mul_f32_e32 v74, 0x3c000000, v74
	v_mul_f32_e32 v75, 0x3c000000, v75
	v_fma_f32 v75, -v74, v74, v75
	v_add_f32_e32 v75, 0x3727c5ac, v75
	v_rsq_f32_e32 v76, v75
	s_nop 0
	v_mul_f32_e64 v236, -v74, v76
	v_pk_fma_f32 v[62:63], v[62:63], v[76:77], v[236:237] op_sel_hi:[1,0,0]
	v_pk_fma_f32 v[64:65], v[64:65], v[76:77], v[236:237] op_sel_hi:[1,0,0]
	v_pk_fma_f32 v[66:67], v[66:67], v[76:77], v[236:237] op_sel_hi:[1,0,0]
	v_pk_fma_f32 v[68:69], v[68:69], v[76:77], v[236:237] op_sel_hi:[1,0,0]
	ds_write_b128 v123, v[62:65]
	v_pk_fma_f32 v[70:71], v[70:71], v[76:77], v[236:237] op_sel_hi:[1,0,0]
	v_pk_fma_f32 v[72:73], v[72:73], v[76:77], v[236:237] op_sel_hi:[1,0,0]
	ds_write_b128 v123, v[66:69] offset:64
	v_pk_fma_f32 v[78:79], v[78:79], v[76:77], v[236:237] op_sel_hi:[1,0,0]
	v_pk_fma_f32 v[80:81], v[80:81], v[76:77], v[236:237] op_sel_hi:[1,0,0]
	ds_write_b128 v123, v[70:73] offset:128
	v_pk_fma_f32 v[86:87], v[86:87], v[76:77], v[236:237] op_sel_hi:[1,0,0]
	v_pk_fma_f32 v[88:89], v[88:89], v[76:77], v[236:237] op_sel_hi:[1,0,0]
	ds_write_b128 v123, v[78:81] offset:192
	v_pk_fma_f32 v[90:91], v[90:91], v[76:77], v[236:237] op_sel_hi:[1,0,0]
	v_pk_fma_f32 v[92:93], v[92:93], v[76:77], v[236:237] op_sel_hi:[1,0,0]
	ds_write_b128 v123, v[86:89] offset:256
	v_pk_fma_f32 v[148:149], v[148:149], v[76:77], v[236:237] op_sel_hi:[1,0,0]
	v_pk_fma_f32 v[150:151], v[150:151], v[76:77], v[236:237] op_sel_hi:[1,0,0]
	ds_write_b128 v123, v[90:93] offset:320
	v_pk_fma_f32 v[82:83], v[82:83], v[76:77], v[236:237] op_sel_hi:[1,0,0]
	v_pk_fma_f32 v[84:85], v[84:85], v[76:77], v[236:237] op_sel_hi:[1,0,0]
	ds_write_b128 v123, v[148:151] offset:384
	ds_write_b128 v123, v[82:85] offset:448
	ds_read_b128 v[62:65], v121
	ds_read_b128 v[66:69], v121 offset:1088
	ds_read_b128 v[70:73], v121 offset:2176
	ds_read_b128 v[74:77], v121 offset:3264
	ds_read_b128 v[78:81], v121 offset:4352
	ds_read_b128 v[82:85], v121 offset:5440
	ds_read_b128 v[86:89], v121 offset:6528
	ds_read_b128 v[90:93], v121 offset:7616
	v_add_u32_e32 v136, 0xffffe400, v118
	s_waitcnt vmcnt(15) lgkmcnt(7)
	v_pk_fma_f32 v[64:65], v[56:57], v[64:65], v[60:61]
	v_pk_fma_f32 v[62:63], v[54:55], v[62:63], v[58:59]
	buffer_store_dwordx4 v[62:65], v136, s[4:7], 0 offen sc0 nt sc1
	v_cmp_lt_i32_e32 vcc, s8, v0
	s_or_b64 s[0:1], vcc, s[0:1]
	s_waitcnt lgkmcnt(6)
	v_pk_fma_f32 v[64:65], v[56:57], v[68:69], v[60:61]
	v_pk_fma_f32 v[62:63], v[54:55], v[66:67], v[58:59]
	v_add_u32_e32 v66, 0xffffe800, v118
	buffer_store_dwordx4 v[62:65], v66, s[4:7], 0 offen sc0 nt sc1
	v_add_u32_e32 v66, 0xffffec00, v118
	s_waitcnt lgkmcnt(5)
	v_pk_fma_f32 v[64:65], v[56:57], v[72:73], v[60:61]
	v_pk_fma_f32 v[62:63], v[54:55], v[70:71], v[58:59]
	buffer_store_dwordx4 v[62:65], v66, s[4:7], 0 offen sc0 nt sc1
	v_add_u32_e32 v66, 0xfffff000, v118
	s_waitcnt lgkmcnt(4)
	v_pk_fma_f32 v[64:65], v[56:57], v[76:77], v[60:61]
	v_pk_fma_f32 v[62:63], v[54:55], v[74:75], v[58:59]
	buffer_store_dwordx4 v[62:65], v66, s[4:7], 0 offen sc0 nt sc1
	v_add_u32_e32 v66, 0xfffff400, v118
	s_waitcnt lgkmcnt(3)
	v_pk_fma_f32 v[64:65], v[56:57], v[80:81], v[60:61]
	v_pk_fma_f32 v[62:63], v[54:55], v[78:79], v[58:59]
	buffer_store_dwordx4 v[62:65], v66, s[4:7], 0 offen sc0 nt sc1
	v_add_u32_e32 v66, 0xfffff800, v118
	s_waitcnt lgkmcnt(2)
	v_pk_fma_f32 v[64:65], v[56:57], v[84:85], v[60:61]
	v_pk_fma_f32 v[62:63], v[54:55], v[82:83], v[58:59]
	buffer_store_dwordx4 v[62:65], v66, s[4:7], 0 offen sc0 nt sc1
	v_add_u32_e32 v66, 0xfffffc00, v118
	s_waitcnt lgkmcnt(1)
	v_pk_fma_f32 v[64:65], v[56:57], v[88:89], v[60:61]
	v_pk_fma_f32 v[62:63], v[54:55], v[86:87], v[58:59]
	buffer_store_dwordx4 v[62:65], v66, s[4:7], 0 offen sc0 nt sc1
	s_waitcnt lgkmcnt(0)
	s_nop 0
	v_pk_fma_f32 v[64:65], v[56:57], v[92:93], v[60:61]
	v_pk_fma_f32 v[62:63], v[54:55], v[90:91], v[58:59]
	buffer_store_dwordx4 v[62:65], v118, s[4:7], 0 offen sc0 nt sc1
	v_add_u32_e32 v118, 0x1000000, v118
	s_nop 0
	v_mov_b32_e32 v62, v0
	s_waitcnt vmcnt(21)
	v_mov_b32_e32 v64, v135
	s_andn2_b64 exec, exec, s[0:1]
	s_cbranch_execnz .LBB1_6
